# t12 + lean conversion-issue fast path (saved pointers advanced in place, no register shuffles)
# baseline (speedup 1.0000x reference)
; DEVI f32x4 ld_nt(const float* p) { return __builtin_nontemporal_load((const f32x4*)p); }
; DEVI void cv_next(const Params& p, int l, int s, int lane, int stride, CvRun& run) {
;     ...
;     run.c = cv_slice(p, l, s, lane); run.left = 0;
;     if ((stride & 511) == 0) {
;         if (s < NS_W13) { const int e = s >> 9, es = stride >> 9; if (e < NE) { run.left = (NE - 1 - e) / es; run.sstep = (long)es * 1024 * 256; run.dstep = (long)es * 512 * 1024; } }
;         else { const int e = (s - NS_W13) >> 8, es = stride >> 8; if (e < NE) { run.left = (NE - 1 - e) / es; run.sstep = (long)es * 256 * 1024; run.dstep = (long)es * 1024 * 256; } } }
; }
; DEVI void cv_issue(const Params& p, int l, int s, int lane, CvRegs& R, CvRun& run) {
;     R.live = s < NS_SLICES ? 1 : 0;
;     if (R.live) { cv_next(p, l, s, lane, (int)gridDim.x * 8, run); R.c = run.c; const int kq = lane >> 3;
;         const float* sp = R.c.src + (size_t)(R.c.k0 + 2 * kq) * R.c.ld;
;         R.a0 = ld_nt(sp); R.b0 = ld_nt(sp + R.c.ld); R.a1 = ld_nt(sp + (size_t)16 * R.c.ld); R.b1 = ld_nt(sp + (size_t)17 * R.c.ld); }
.LBB0_693:
	s_and_b64 vcc, exec, s[16:17]
	s_cbranch_vccz .LBB0_695
	s_lshl_b64 s[6:7], s[26:27], 1
	v_lshl_add_u64 v[170:171], s[28:29], 2, v[170:171]
	v_lshl_add_u64 v[172:173], v[172:173], 0, s[6:7]
	s_add_i32 s56, s56, -1
	s_mov_b32 s8, s60
	s_mov_b32 s94, s59
	s_mov_b32 s10, s58
	s_mov_b32 s95, s55
	s_mov_b32 s6, s57
	v_add_u32_e32 v252, s58, v128
	s_ashr_i32 s7, s57, 31
	v_mad_i64_i32 v[252:253], s[16:17], v252, s57, 0
	v_lshl_add_u64 v[252:253], v[252:253], 2, v[170:171]
	s_lshl_b64 s[16:17], s[6:7], 2
	v_lshl_add_u64 v[254:255], v[252:253], 0, s[16:17]
	global_load_dwordx4 v[154:157], v[252:253], off nt
	global_load_dwordx4 v[158:161], v[254:255], off nt
	v_mad_i64_i32 v[252:253], s[18:19], s57, 60, v[254:255]
	v_lshl_add_u64 v[254:255], v[252:253], 0, s[16:17]
	global_load_dwordx4 v[162:165], v[252:253], off nt
	global_load_dwordx4 v[166:169], v[254:255], off nt
	s_branch .LBB0_696

; DEVI void cv_finish(char* img  , int lane, const CvRegs& R) {
;     ...
;     const int n = lane >> 1, half = lane & 1; u32x4 w0, w1;
; #pragma unroll
;     for (int j = 0; j < 4; ++j) { w0[j] = *(const unsigned*)(img + n * 68 + half * 32 + j * 4); w1[j] = *(const unsigned*)(img + n * 68 + half * 32 + 16 + j * 4); }
;     const int row = R.c.perm ? R.c.r0 + 128 * ((n >> 3) & 1) + 16 * ((n >> 2) & 1) + 4 * (n >> 4) + (n & 3) : R.c.r0 + 128 * ((n >> 2) & 1) + 4 * (n >> 3) + (n & 3);
;     bf16_t* d = R.c.dst + (size_t)row * R.c.K + R.c.k0 + half * 16;
;     __builtin_nontemporal_store(w0, (u32x4*)d); __builtin_nontemporal_store(w1, (u32x4*)(d + 8));
;     asm volatile("" ::: "memory"); __builtin_amdgcn_wave_barrier();
.Lmy_cvj_a:
	ds_read2_b32 v[82:83], v84 offset1:1
	ds_read2_b32 v[86:87], v84 offset0:4 offset1:5
	ds_read2_b32 v[88:89], v84 offset0:6 offset1:7
	ds_read2_b32 v[84:85], v84 offset0:2 offset1:3
	v_add_u32_e32 v90, s8, v90
	v_mad_i64_i32 v[90:91], s[6:7], v90, s94, 0
	v_lshl_add_u64 v[90:91], v[90:91], 1, v[172:173]
	s_ashr_i32 s11, s10, 31
	v_lshl_add_u64 v[90:91], s[10:11], 1, v[90:91]
	v_lshlrev_b32_e32 v174, 1, v180
	v_lshl_add_u64 v[90:91], v[90:91], 0, v[174:175]
	s_waitcnt lgkmcnt(0)
	global_store_dwordx4 v[90:91], v[82:85], off nt
	global_store_dwordx4 v[90:91], v[86:89], off offset:16 nt
	s_waitcnt vmcnt(2)
	s_cbranch_execz .LBB0_701
	s_branch .LBB0_702
